# scatter dst/src loads issued right after the histogram-matrix phase so they overlap the bucket scan
# speedup vs baseline: 1.0187x; 1.0060x over previous
_Z14scatter_kernelPKiS0_S0_PiP15HIP_vector_typeIiLj2EE:
	s_load_dwordx4 s[52:55], s[0:1], 0x0
	s_load_dwordx4 s[12:15], s[0:1], 0x18
	s_movk_i32 s3, 0x31f
	v_cmp_lt_u32_e64 s[4:5], s3, v0
	s_movk_i32 s3, 0x320
	v_cmp_gt_u32_e32 vcc, s3, v0
	v_mov_b32_e32 v80, 0
	v_lshlrev_b32_e32 v2, 3, v0
	v_mov_b32_e32 v1, 0
	v_mov_b32_e32 v79, 0
	v_mov_b32_e32 v78, 0
	v_mov_b32_e32 v3, 0
	v_mov_b32_e32 v81, 0
	s_and_saveexec_b64 s[10:11], vcc
	s_cbranch_execz .LBB1_3
	s_load_dwordx2 s[6:7], s[0:1], 0x10
	v_mov_b32_e32 v3, 0
	s_mov_b64 s[8:9], 0x19000
	s_mov_b32 s3, 0
	s_mov_b32 s18, 0xfffeb000
	s_waitcnt lgkmcnt(0)
	v_lshl_add_u64 v[4:5], s[6:7], 0, v[2:3]
	v_lshl_add_u64 v[4:5], v[4:5], 0, s[8:9]
	s_mov_b32 s19, 0xfffec000
	s_mov_b32 s20, 0xfffee000
	s_mov_b32 s21, 0xfffef000
	s_mov_b32 s22, 0xffff1000
	s_mov_b32 s23, 0xffff2000
	s_mov_b32 s24, 0xffff4000
	s_mov_b32 s25, 0xffff6000
	s_mov_b32 s26, 0xffff7000
	s_movk_i32 s27, 0x9000
	s_movk_i32 s28, 0xa000
	s_movk_i32 s29, 0xc000
	s_movk_i32 s30, 0xd000
	s_movk_i32 s31, 0xf000
	s_movk_i32 s33, 0x1000
	s_movk_i32 s34, 0x3000
	s_movk_i32 s35, 0x4000
	s_movk_i32 s36, 0x6000
	s_movk_i32 s37, 0x7000
	s_mov_b32 s38, 0x9000
	s_mov_b32 s39, 0xa000
	s_mov_b32 s40, 0xc000
	s_mov_b32 s41, 0xe000
	s_mov_b32 s42, 0xf000
	s_mov_b32 s43, 0x11000
	s_mov_b32 s44, 0x12000
	s_mov_b32 s45, 0x14000
	s_mov_b32 s46, 0x15000
	s_mov_b32 s47, 0x17000
	s_mov_b64 s[16:17], 0x32000
	v_mov_b32_e32 v81, v3
	v_mov_b32_e32 v79, v3
	v_mov_b32_e32 v78, v3
	v_mov_b32_e32 v1, v3
	v_mov_b32_e32 v80, v3

.LBB1_3:
	s_or_b64 exec, exec, s[10:11]
	s_mul_i32 s56, s2, 0x2710
	s_mov_b64 s[58:59], 0x1000
	s_mov_b64 s[60:61], 0x9000
	v_add_u32_e32 v120, s56, v0
	v_mov_b32_e32 v121, 0
	v_lshlrev_b64 v[120:121], 2, v[120:121]
	v_cmp_gt_u32_e32 vcc, 0x310, v0
	s_waitcnt lgkmcnt(0)
	v_lshl_add_u64 v[122:123], s[52:53], 0, v[120:121]
	v_lshl_add_u64 v[120:121], s[54:55], 0, v[120:121]
	v_lshl_add_u64 v[124:125], v[120:121], 0, s[60:61]
	v_lshl_add_u64 v[126:127], v[122:123], 0, s[60:61]
	s_and_saveexec_b64 s[62:63], vcc
	global_load_dword v109, v[124:125], off
	global_load_dword v119, v[126:127], off
	s_or_b64 exec, exec, s[62:63]
	global_load_dword v100, v[120:121], off
	v_lshl_add_u64 v[120:121], v[120:121], 0, s[58:59]
	global_load_dword v101, v[120:121], off
	v_lshl_add_u64 v[120:121], v[120:121], 0, s[58:59]
	global_load_dword v102, v[120:121], off
	v_lshl_add_u64 v[120:121], v[120:121], 0, s[58:59]
	global_load_dword v103, v[120:121], off
	v_lshl_add_u64 v[120:121], v[120:121], 0, s[58:59]
	global_load_dword v104, v[120:121], off
	v_lshl_add_u64 v[120:121], v[120:121], 0, s[58:59]
	global_load_dword v105, v[120:121], off
	v_lshl_add_u64 v[120:121], v[120:121], 0, s[58:59]
	global_load_dword v106, v[120:121], off
	v_lshl_add_u64 v[120:121], v[120:121], 0, s[58:59]
	global_load_dword v107, v[120:121], off
	v_lshl_add_u64 v[120:121], v[120:121], 0, s[58:59]
	global_load_dword v108, v[120:121], off
	global_load_dword v110, v[122:123], off
	v_lshl_add_u64 v[122:123], v[122:123], 0, s[58:59]
	global_load_dword v111, v[122:123], off
	v_lshl_add_u64 v[122:123], v[122:123], 0, s[58:59]
	global_load_dword v112, v[122:123], off
	v_lshl_add_u64 v[122:123], v[122:123], 0, s[58:59]
	global_load_dword v113, v[122:123], off
	v_lshl_add_u64 v[122:123], v[122:123], 0, s[58:59]
	global_load_dword v114, v[122:123], off
	v_lshl_add_u64 v[122:123], v[122:123], 0, s[58:59]
	global_load_dword v115, v[122:123], off
	v_lshl_add_u64 v[122:123], v[122:123], 0, s[58:59]
	global_load_dword v116, v[122:123], off
	v_lshl_add_u64 v[122:123], v[122:123], 0, s[58:59]
	global_load_dword v117, v[122:123], off
	v_lshl_add_u64 v[122:123], v[122:123], 0, s[58:59]
	global_load_dword v118, v[122:123], off
	v_mbcnt_lo_u32_b32 v4, -1, 0
	v_mbcnt_hi_u32_b32 v6, -1, v4
	v_and_b32_e32 v7, 64, v6
	v_add_u32_e32 v4, -1, v6
	v_cmp_lt_i32_e32 vcc, v4, v7
	v_add_u32_e32 v5, v3, v81
	v_and_b32_e32 v10, 63, v0
	v_cndmask_b32_e32 v4, v4, v6, vcc
	v_lshlrev_b32_e32 v8, 2, v4
	v_add_u32_e32 v4, v1, v80
	ds_bpermute_b32 v9, v8, v5
	ds_bpermute_b32 v8, v8, v4
	v_cmp_eq_u32_e32 vcc, 0, v10
	v_add_u32_e32 v11, -2, v6
	s_load_dwordx4 s[8:11], s[0:1], 0x0
	s_waitcnt lgkmcnt(0)
	v_cndmask_b32_e64 v9, v9, 0, vcc
	v_cndmask_b32_e64 v8, v8, 0, vcc
	v_cmp_lt_i32_e32 vcc, v11, v7
	v_add_u32_e32 v9, v9, v5
	v_add_u32_e32 v8, v8, v4
	v_cndmask_b32_e32 v11, v11, v6, vcc
	v_lshlrev_b32_e32 v11, 2, v11
	ds_bpermute_b32 v12, v11, v9
	ds_bpermute_b32 v11, v11, v8
	v_cmp_gt_u32_e32 vcc, 2, v10
	s_waitcnt lgkmcnt(1)
	s_nop 0
	v_cndmask_b32_e64 v12, v12, 0, vcc
	v_add_u32_e32 v9, v12, v9
	v_add_u32_e32 v12, -4, v6
	s_waitcnt lgkmcnt(0)
	v_cndmask_b32_e64 v11, v11, 0, vcc
	v_cmp_lt_i32_e32 vcc, v12, v7
	v_add_u32_e32 v8, v11, v8
	s_nop 0
	v_cndmask_b32_e32 v12, v12, v6, vcc
	v_lshlrev_b32_e32 v12, 2, v12
	ds_bpermute_b32 v13, v12, v9
	ds_bpermute_b32 v11, v12, v8
	v_cmp_gt_u32_e32 vcc, 4, v10
	s_waitcnt lgkmcnt(1)
	s_nop 0
	v_cndmask_b32_e64 v12, v13, 0, vcc
	v_add_u32_e32 v9, v12, v9
	v_add_u32_e32 v12, -8, v6
	s_waitcnt lgkmcnt(0)
	v_cndmask_b32_e64 v11, v11, 0, vcc
	v_cmp_lt_i32_e32 vcc, v12, v7
	v_add_u32_e32 v8, v11, v8
	s_nop 0
	v_cndmask_b32_e32 v12, v12, v6, vcc
	v_lshlrev_b32_e32 v12, 2, v12
	ds_bpermute_b32 v13, v12, v9
	ds_bpermute_b32 v11, v12, v8
	v_cmp_gt_u32_e32 vcc, 8, v10
	s_waitcnt lgkmcnt(1)
	s_nop 0
	v_cndmask_b32_e64 v12, v13, 0, vcc
	v_add_u32_e32 v9, v12, v9
	v_add_u32_e32 v12, -16, v6
	s_waitcnt lgkmcnt(0)
	v_cndmask_b32_e64 v11, v11, 0, vcc
	v_cmp_lt_i32_e32 vcc, v12, v7
	v_add_u32_e32 v8, v11, v8
	s_nop 0
	v_cndmask_b32_e32 v12, v12, v6, vcc
	v_lshlrev_b32_e32 v12, 2, v12
	ds_bpermute_b32 v13, v12, v9
	ds_bpermute_b32 v11, v12, v8
	v_cmp_gt_u32_e32 vcc, 16, v10
	s_waitcnt lgkmcnt(1)
	s_nop 0
	v_cndmask_b32_e64 v12, v13, 0, vcc
	v_add_u32_e32 v9, v12, v9
	v_subrev_u32_e32 v12, 32, v6
	s_waitcnt lgkmcnt(0)
	v_cndmask_b32_e64 v11, v11, 0, vcc
	v_cmp_lt_i32_e32 vcc, v12, v7
	v_add_u32_e32 v8, v11, v8
	v_lshrrev_b32_e32 v11, 6, v0
	v_cndmask_b32_e32 v6, v12, v6, vcc
	v_lshlrev_b32_e32 v6, 2, v6
	ds_bpermute_b32 v7, v6, v9
	ds_bpermute_b32 v12, v6, v8
	v_cmp_gt_u32_e32 vcc, 32, v10
	s_waitcnt lgkmcnt(1)
	s_nop 0
	v_cndmask_b32_e64 v6, v7, 0, vcc
	s_waitcnt lgkmcnt(0)
	v_cndmask_b32_e64 v7, v12, 0, vcc
	v_add_u32_e32 v6, v6, v9
	v_add_u32_e32 v7, v7, v8
	v_cmp_eq_u32_e32 vcc, 63, v10
	s_and_saveexec_b64 s[0:1], vcc
	v_mov_b32_e32 v8, 0x1e6a0
	v_lshl_add_u32 v8, v11, 2, v8
	ds_write2_b32 v8, v7, v6 offset1:16
	s_or_b64 exec, exec, s[0:1]
	v_cmp_lt_u32_e32 vcc, 63, v0
	v_mov_b32_e32 v8, 0
	v_mov_b32_e32 v9, 0
	s_waitcnt lgkmcnt(0)
	s_barrier
	s_and_saveexec_b64 s[0:1], vcc
	s_cbranch_execz .LBB1_15
	v_add_u32_e32 v8, -1, v11
	v_cmp_lt_u32_e32 vcc, 6, v8
	v_mov_b32_e32 v9, 0
	v_mov_b32_e32 v8, 0
	v_mov_b32_e32 v10, 0
	s_and_saveexec_b64 s[6:7], vcc
	s_cbranch_execz .LBB1_10
	v_and_b32_e32 v10, 8, v11
	s_mov_b32 s3, 0
	s_mov_b32 s18, 0x1e6a0
	s_mov_b64 s[16:17], 0
	v_mov_b32_e32 v8, 0
	v_mov_b32_e32 v9, 0

.Lscat_loads:
	v_cmp_gt_u32_e32 vcc, 0x310, v0
	v_add_u32_e32 v13, s4, v0
	s_waitcnt vmcnt(17)
	v_ashrrev_i32_e32 v50, 6, v100
	v_lshl_add_u32 v60, v50, 2, v1
	ds_add_rtn_u32 v60, v60, v6
	v_lshlrev_b32_e32 v100, 20, v100
	v_mov_b32_e32 v70, v13
	v_and_or_b32 v100, v100, s5, v70
	s_waitcnt vmcnt(16)
	v_ashrrev_i32_e32 v51, 6, v101
	v_lshl_add_u32 v61, v51, 2, v1
	ds_add_rtn_u32 v61, v61, v6
	v_lshlrev_b32_e32 v101, 20, v101
	v_add_u32_e32 v71, 0x400, v13
	v_and_or_b32 v101, v101, s5, v71
	s_waitcnt vmcnt(15)
	v_ashrrev_i32_e32 v52, 6, v102
	v_lshl_add_u32 v62, v52, 2, v1
	ds_add_rtn_u32 v62, v62, v6
	v_lshlrev_b32_e32 v102, 20, v102
	v_add_u32_e32 v72, 0x800, v13
	v_and_or_b32 v102, v102, s5, v72
	s_waitcnt vmcnt(14)
	v_ashrrev_i32_e32 v53, 6, v103
	v_lshl_add_u32 v63, v53, 2, v1
	ds_add_rtn_u32 v63, v63, v6
	v_lshlrev_b32_e32 v103, 20, v103
	v_add_u32_e32 v73, 0xc00, v13
	v_and_or_b32 v103, v103, s5, v73
	s_waitcnt vmcnt(13)
	v_ashrrev_i32_e32 v54, 6, v104
	v_lshl_add_u32 v64, v54, 2, v1
	ds_add_rtn_u32 v64, v64, v6
	v_lshlrev_b32_e32 v104, 20, v104
	v_add_u32_e32 v74, 0x1000, v13
	v_and_or_b32 v104, v104, s5, v74
	s_waitcnt vmcnt(12)
	v_ashrrev_i32_e32 v55, 6, v105
	v_lshl_add_u32 v65, v55, 2, v1
	ds_add_rtn_u32 v65, v65, v6
	v_lshlrev_b32_e32 v105, 20, v105
	v_add_u32_e32 v75, 0x1400, v13
	v_and_or_b32 v105, v105, s5, v75
	s_waitcnt vmcnt(11)
	v_ashrrev_i32_e32 v56, 6, v106
	v_lshl_add_u32 v66, v56, 2, v1
	ds_add_rtn_u32 v66, v66, v6
	v_lshlrev_b32_e32 v106, 20, v106
	v_add_u32_e32 v76, 0x1800, v13
	v_and_or_b32 v106, v106, s5, v76
	s_waitcnt vmcnt(10)
	v_ashrrev_i32_e32 v57, 6, v107
	v_lshl_add_u32 v67, v57, 2, v1
	ds_add_rtn_u32 v67, v67, v6
	v_lshlrev_b32_e32 v107, 20, v107
	v_add_u32_e32 v77, 0x1c00, v13
	v_and_or_b32 v107, v107, s5, v77
	s_waitcnt vmcnt(9)
	v_ashrrev_i32_e32 v58, 6, v108
	v_lshl_add_u32 v68, v58, 2, v1
	ds_add_rtn_u32 v68, v68, v6
	v_lshlrev_b32_e32 v108, 20, v108
	v_add_u32_e32 v78, 0x2000, v13
	v_and_or_b32 v108, v108, s5, v78
	s_and_saveexec_b64 s[0:1], vcc
	v_ashrrev_i32_e32 v59, 6, v109
	v_lshl_add_u32 v69, v59, 2, v1
	ds_add_rtn_u32 v69, v69, v6
	v_lshlrev_b32_e32 v109, 20, v109
	v_add_u32_e32 v79, 0x2400, v13
	v_and_or_b32 v109, v109, s5, v79
	s_or_b64 exec, exec, s[0:1]
	s_waitcnt lgkmcnt(0)
	v_lshlrev_b32_e32 v70, 2, v60
	v_lshl_add_u32 v60, v60, 1, s6
	ds_write_b32 v70, v100
	ds_write_b16 v60, v50
	s_waitcnt vmcnt(8)
	ds_write_b32 v70, v110 offset:40000
	v_lshlrev_b32_e32 v71, 2, v61
	v_lshl_add_u32 v61, v61, 1, s6
	ds_write_b32 v71, v101
	ds_write_b16 v61, v51
	s_waitcnt vmcnt(7)
	ds_write_b32 v71, v111 offset:40000
	v_lshlrev_b32_e32 v72, 2, v62
	v_lshl_add_u32 v62, v62, 1, s6
	ds_write_b32 v72, v102
	ds_write_b16 v62, v52
	s_waitcnt vmcnt(6)
	ds_write_b32 v72, v112 offset:40000
	v_lshlrev_b32_e32 v73, 2, v63
	v_lshl_add_u32 v63, v63, 1, s6
	ds_write_b32 v73, v103
	ds_write_b16 v63, v53
	s_waitcnt vmcnt(5)
	ds_write_b32 v73, v113 offset:40000
	v_lshlrev_b32_e32 v74, 2, v64
	v_lshl_add_u32 v64, v64, 1, s6
	ds_write_b32 v74, v104
	ds_write_b16 v64, v54
	s_waitcnt vmcnt(4)
	ds_write_b32 v74, v114 offset:40000
	v_lshlrev_b32_e32 v75, 2, v65
	v_lshl_add_u32 v65, v65, 1, s6
	ds_write_b32 v75, v105
	ds_write_b16 v65, v55
	s_waitcnt vmcnt(3)
	ds_write_b32 v75, v115 offset:40000
	v_lshlrev_b32_e32 v76, 2, v66
	v_lshl_add_u32 v66, v66, 1, s6
	ds_write_b32 v76, v106
	ds_write_b16 v66, v56
	s_waitcnt vmcnt(2)
	ds_write_b32 v76, v116 offset:40000
	v_lshlrev_b32_e32 v77, 2, v67
	v_lshl_add_u32 v67, v67, 1, s6
	ds_write_b32 v77, v107
	ds_write_b16 v67, v57
	s_waitcnt vmcnt(1)
	ds_write_b32 v77, v117 offset:40000
	v_lshlrev_b32_e32 v78, 2, v68
	v_lshl_add_u32 v68, v68, 1, s6
	ds_write_b32 v78, v108
	ds_write_b16 v68, v58
	s_waitcnt vmcnt(0)
	ds_write_b32 v78, v118 offset:40000
	s_and_saveexec_b64 s[0:1], vcc
	v_lshlrev_b32_e32 v79, 2, v69
	v_lshl_add_u32 v69, v69, 1, s6
	ds_write_b32 v79, v109
	ds_write_b16 v69, v59
	ds_write_b32 v79, v119 offset:40000
	s_or_b64 exec, exec, s[0:1]
	v_add_u32_e32 v1, 0x13880, v10
	v_lshlrev_b32_e32 v2, 2, v0
	s_mov_b64 s[0:1], 0
	s_movk_i32 s2, 0x230f
	s_waitcnt lgkmcnt(0)
	s_barrier
